# speedup vs baseline: 1.0244x; 1.0092x over previous
_Z9ln_kernelILi2EEvPKiPKfS3_PfS3_S3_PDF16_:
	s_load_dwordx8 s[4:11], s[0:1], 0x8
	v_and_b32_e32 v12, 63, v0
	v_lshrrev_b32_e32 v0, 6, v0
	v_lshl_or_b32 v6, s2, 2, v0
	v_ashrrev_i32_e32 v7, 31, v6
	v_lshlrev_b64 v[2:3], 11, v[6:7]
	v_mov_b32_e32 v1, 0
	s_waitcnt lgkmcnt(0)
	v_lshl_add_u64 v[8:9], s[4:5], 0, v[2:3]
	v_lshlrev_b32_e32 v4, 3, v12
	v_mov_b32_e32 v5, v1
	v_lshl_add_u64 v[8:9], v[8:9], 0, v[4:5]
	s_mov_b64 s[2:3], 0x400000
	v_lshl_add_u64 v[10:11], v[8:9], 0, s[2:3]
	s_mov_b32 s2, 0x400000
	global_load_dwordx2 v[16:17], v[8:9], off
	global_load_dwordx2 v[18:19], v[8:9], off offset:512
	global_load_dwordx2 v[20:21], v[8:9], off offset:1024
	global_load_dwordx2 v[22:23], v[8:9], off offset:1536
	v_add_co_u32_e32 v8, vcc, s2, v8
	global_load_dwordx2 v[24:25], v[10:11], off offset:512
	global_load_dwordx2 v[26:27], v[10:11], off offset:1024
	global_load_dwordx2 v[28:29], v[10:11], off offset:1536
	v_addc_co_u32_e32 v9, vcc, 0, v9, vcc
	global_load_dwordx2 v[30:31], v[8:9], off
	v_lshlrev_b64 v[6:7], 12, v[6:7]
	v_lshlrev_b32_e32 v0, 4, v12
	v_lshl_add_u64 v[6:7], s[8:9], 0, v[6:7]
	v_lshl_add_u64 v[6:7], v[6:7], 0, v[0:1]
	global_load_dwordx4 v[8:11], v[6:7], off offset:1024
	global_load_dwordx4 v[12:15], v0, s[6:7] offset:1024
	global_load_dwordx4 v[64:67], v[6:7], off
	global_load_dwordx4 v[68:71], v[6:7], off offset:2048
	global_load_dwordx4 v[72:75], v[6:7], off offset:3072
	global_load_dwordx4 v[76:79], v0, s[6:7] offset:2048
	global_load_dwordx4 v[80:83], v0, s[6:7]
	global_load_dwordx4 v[84:87], v0, s[6:7] offset:3072
	s_waitcnt vmcnt(15)
	v_cvt_f32_f16_e32 v32, v16
	s_waitcnt vmcnt(14)
	v_cvt_f32_f16_e32 v36, v18
	v_cvt_f32_f16_sdwa v37, v18 dst_sel:DWORD dst_unused:UNUSED_PAD src0_sel:WORD_1
	v_cvt_f32_f16_e32 v38, v19
	v_cvt_f32_f16_sdwa v39, v19 dst_sel:DWORD dst_unused:UNUSED_PAD src0_sel:WORD_1
	s_waitcnt vmcnt(13)
	v_cvt_f32_f16_e32 v40, v20
	v_cvt_f32_f16_sdwa v41, v20 dst_sel:DWORD dst_unused:UNUSED_PAD src0_sel:WORD_1
	v_cvt_f32_f16_e32 v42, v21
	v_cvt_f32_f16_sdwa v43, v21 dst_sel:DWORD dst_unused:UNUSED_PAD src0_sel:WORD_1
	s_waitcnt vmcnt(12)
	v_cvt_f32_f16_e32 v44, v22
	v_cvt_f32_f16_sdwa v45, v22 dst_sel:DWORD dst_unused:UNUSED_PAD src0_sel:WORD_1
	v_cvt_f32_f16_e32 v46, v23
	v_cvt_f32_f16_sdwa v47, v23 dst_sel:DWORD dst_unused:UNUSED_PAD src0_sel:WORD_1
	s_waitcnt vmcnt(11)
	v_cvt_f32_f16_e32 v20, v24
	v_cvt_f32_f16_sdwa v21, v24 dst_sel:DWORD dst_unused:UNUSED_PAD src0_sel:WORD_1
	v_cvt_f32_f16_e32 v22, v25
	v_cvt_f32_f16_sdwa v23, v25 dst_sel:DWORD dst_unused:UNUSED_PAD src0_sel:WORD_1
	s_waitcnt vmcnt(10)
	v_cvt_f32_f16_e32 v24, v26
	v_cvt_f32_f16_sdwa v25, v26 dst_sel:DWORD dst_unused:UNUSED_PAD src0_sel:WORD_1
	v_cvt_f32_f16_e32 v26, v27
	v_cvt_f32_f16_sdwa v27, v27 dst_sel:DWORD dst_unused:UNUSED_PAD src0_sel:WORD_1
	s_waitcnt vmcnt(9)
	v_cvt_f32_f16_e32 v48, v28
	v_cvt_f32_f16_sdwa v49, v28 dst_sel:DWORD dst_unused:UNUSED_PAD src0_sel:WORD_1
	v_cvt_f32_f16_e32 v28, v29
	v_cvt_f32_f16_sdwa v29, v29 dst_sel:DWORD dst_unused:UNUSED_PAD src0_sel:WORD_1
	v_cvt_f32_f16_sdwa v33, v16 dst_sel:DWORD dst_unused:UNUSED_PAD src0_sel:WORD_1
	v_cvt_f32_f16_e32 v34, v17
	v_cvt_f32_f16_sdwa v35, v17 dst_sel:DWORD dst_unused:UNUSED_PAD src0_sel:WORD_1
	s_waitcnt vmcnt(8)
	v_cvt_f32_f16_e32 v50, v30
	v_cvt_f32_f16_sdwa v51, v30 dst_sel:DWORD dst_unused:UNUSED_PAD src0_sel:WORD_1
	v_cvt_f32_f16_e32 v52, v31
	v_cvt_f32_f16_sdwa v53, v31 dst_sel:DWORD dst_unused:UNUSED_PAD src0_sel:WORD_1
	s_waitcnt vmcnt(0)
	v_mov_b32_e32 v16, v64
	v_mov_b32_e32 v17, v65
	v_mov_b32_e32 v18, v66
	v_mov_b32_e32 v19, v67
	v_pk_add_f32 v[36:37], v[36:37], v[20:21]
	v_pk_add_f32 v[38:39], v[38:39], v[22:23]
	v_mov_b32_e32 v20, v68
	v_mov_b32_e32 v21, v69
	v_mov_b32_e32 v22, v70
	v_mov_b32_e32 v23, v71
	v_pk_add_f32 v[40:41], v[40:41], v[24:25]
	v_pk_add_f32 v[42:43], v[42:43], v[26:27]
	v_mov_b32_e32 v24, v72
	v_mov_b32_e32 v25, v73
	v_mov_b32_e32 v26, v74
	v_mov_b32_e32 v27, v75
	v_pk_add_f32 v[46:47], v[46:47], v[28:29]
	v_mov_b32_e32 v28, v76
	v_mov_b32_e32 v29, v77
	v_mov_b32_e32 v30, v78
	v_mov_b32_e32 v31, v79
	s_waitcnt vmcnt(5)
	v_pk_add_f32 v[36:37], v[8:9], v[36:37]
	v_pk_add_f32 v[38:39], v[10:11], v[38:39]
	v_mov_b32_e32 v8, v80
	v_mov_b32_e32 v9, v81
	v_mov_b32_e32 v10, v82
	v_mov_b32_e32 v11, v83
	v_pk_add_f32 v[44:45], v[44:45], v[48:49]
	v_pk_add_f32 v[48:49], v[32:33], v[50:51]
	v_pk_add_f32 v[50:51], v[34:35], v[52:53]
	v_mov_b32_e32 v32, v84
	v_mov_b32_e32 v33, v85
	v_mov_b32_e32 v34, v86
	v_mov_b32_e32 v35, v87
	s_waitcnt vmcnt(6)
	v_pk_add_f32 v[12:13], v[12:13], v[36:37]
	v_pk_add_f32 v[14:15], v[14:15], v[38:39]
	s_load_dwordx4 s[4:7], s[0:1], 0x28
	s_mov_b32 s0, 0xf800000
	s_waitcnt lgkmcnt(0)
	v_lshl_add_u64 v[2:3], s[6:7], 0, v[2:3]
	s_waitcnt vmcnt(4)
	v_pk_add_f32 v[20:21], v[20:21], v[40:41]
	v_pk_add_f32 v[22:23], v[22:23], v[42:43]
	v_pk_add_f32 v[40:41], v[16:17], v[48:49]
	v_pk_add_f32 v[42:43], v[18:19], v[50:51]
	s_waitcnt vmcnt(3)
	v_pk_add_f32 v[24:25], v[24:25], v[44:45]
	v_pk_add_f32 v[26:27], v[26:27], v[46:47]
	s_waitcnt vmcnt(2)
	v_pk_add_f32 v[16:17], v[28:29], v[20:21]
	v_pk_add_f32 v[18:19], v[30:31], v[22:23]
	s_waitcnt vmcnt(1)
	v_pk_add_f32 v[8:9], v[8:9], v[40:41]
	v_pk_add_f32 v[10:11], v[10:11], v[42:43]
	v_mov_b32_e32 v28, v13
	v_mov_b32_e32 v29, v15
	s_waitcnt vmcnt(0)
	v_pk_add_f32 v[20:21], v[32:33], v[24:25]
	v_pk_add_f32 v[22:23], v[34:35], v[26:27]
	v_mov_b32_e32 v24, v8
	v_mov_b32_e32 v25, v10
	v_mov_b32_e32 v26, v9
	v_mov_b32_e32 v27, v11
	v_pk_add_f32 v[24:25], v[24:25], v[26:27]
	v_mov_b32_e32 v26, v12
	v_mov_b32_e32 v27, v14
	v_pk_add_f32 v[26:27], v[26:27], v[28:29]
	v_add_f32_e32 v1, v24, v25
	v_pk_add_f32 v[26:27], v[26:27], v[26:27] op_sel:[0,1] op_sel_hi:[1,0]
	v_pk_add_f32 v[28:29], v[16:17], v[16:17] op_sel:[0,1] op_sel_hi:[1,0]
	v_pk_add_f32 v[30:31], v[18:19], v[18:19] op_sel:[0,1] op_sel_hi:[1,0]
	v_add_f32_e32 v24, 0, v1
	v_mov_b32_e32 v25, v20
	v_mov_b32_e32 v27, v21
	v_mov_b32_e32 v29, v22
	v_mov_b32_e32 v31, v23
	v_pk_add_f32 v[24:25], v[24:25], v[26:27]
	v_pk_add_f32 v[26:27], v[28:29], v[30:31]
	s_nop 0
	v_pk_add_f32 v[24:25], v[24:25], v[26:27]
	s_nop 0
	v_add_f32_e32 v1, v24, v25
	v_mbcnt_lo_u32_b32 v24, -1, 0
	v_mbcnt_hi_u32_b32 v24, -1, v24
	v_and_b32_e32 v25, 64, v24
	v_add_u32_e32 v25, 64, v25
	v_xor_b32_e32 v26, 32, v24
	v_cmp_lt_i32_e32 vcc, v26, v25
	s_nop 1
	v_cndmask_b32_e32 v26, v24, v26, vcc
	v_lshlrev_b32_e32 v52, 2, v26
	v_mov_b32_e32 v26, v1
	s_waitcnt lgkmcnt(0)
	s_nop 1
	v_permlane32_swap_b32_e32 v1, v26
	v_add_f32_e32 v1, v1, v26
	v_xor_b32_e32 v26, 16, v24
	v_cmp_lt_i32_e32 vcc, v26, v25
	s_nop 1
	v_cndmask_b32_e32 v26, v24, v26, vcc
	v_lshlrev_b32_e32 v53, 2, v26
	v_mov_b32_e32 v26, v1
	s_waitcnt lgkmcnt(0)
	s_nop 1
	v_permlane16_swap_b32_e32 v1, v26
	v_add_f32_e32 v1, v1, v26
	v_xor_b32_e32 v26, 8, v24
	v_cmp_lt_i32_e32 vcc, v26, v25
	s_nop 1
	v_cndmask_b32_e32 v26, v24, v26, vcc
	v_lshlrev_b32_e32 v54, 2, v26
	s_waitcnt lgkmcnt(0)
	s_nop 1
	v_add_f32_dpp v1, v1, v1 row_ror:8 row_mask:0xf bank_mask:0xf
	v_xor_b32_e32 v26, 4, v24
	v_cmp_lt_i32_e32 vcc, v26, v25
	s_nop 1
	v_cndmask_b32_e32 v26, v24, v26, vcc
	v_lshlrev_b32_e32 v55, 2, v26
	s_waitcnt lgkmcnt(0)
	s_nop 1
	v_add_f32_dpp v1, v1, v1 row_ror:4 row_mask:0xf bank_mask:0xf
	v_xor_b32_e32 v26, 2, v24
	v_cmp_lt_i32_e32 vcc, v26, v25
	s_nop 1
	v_cndmask_b32_e32 v26, v24, v26, vcc
	v_lshlrev_b32_e32 v56, 2, v26
	s_waitcnt lgkmcnt(0)
	s_nop 1
	v_add_f32_dpp v1, v1, v1 row_ror:2 row_mask:0xf bank_mask:0xf
	v_xor_b32_e32 v26, 1, v24
	v_cmp_lt_i32_e32 vcc, v26, v25
	s_nop 1
	v_cndmask_b32_e32 v24, v24, v26, vcc
	v_lshlrev_b32_e32 v57, 2, v24
	s_waitcnt lgkmcnt(0)
	s_nop 1
	v_add_f32_dpp v1, v1, v1 row_ror:1 row_mask:0xf bank_mask:0xf
	v_mul_f32_e32 v24, 0x3a800000, v1
	v_pk_add_f32 v[36:37], v[8:9], v[24:25] op_sel_hi:[1,0] neg_lo:[0,1] neg_hi:[0,1]
	v_pk_add_f32 v[38:39], v[10:11], v[24:25] op_sel_hi:[1,0] neg_lo:[0,1] neg_hi:[0,1]
	v_mov_b32_e32 v28, v37
	v_mov_b32_e32 v29, v39
	v_pk_add_f32 v[40:41], v[12:13], v[24:25] op_sel_hi:[1,0] neg_lo:[0,1] neg_hi:[0,1]
	v_pk_add_f32 v[42:43], v[14:15], v[24:25] op_sel_hi:[1,0] neg_lo:[0,1] neg_hi:[0,1]
	v_mov_b32_e32 v26, v36
	v_mov_b32_e32 v27, v38
	v_pk_mul_f32 v[28:29], v[28:29], v[28:29]
	v_mov_b32_e32 v30, v41
	v_mov_b32_e32 v31, v43
	v_pk_fma_f32 v[26:27], v[26:27], v[26:27], v[28:29]
	v_mov_b32_e32 v28, v40
	v_mov_b32_e32 v29, v42
	v_pk_mul_f32 v[30:31], v[30:31], v[30:31]
	v_pk_add_f32 v[44:45], v[16:17], v[24:25] op_sel_hi:[1,0] neg_lo:[0,1] neg_hi:[0,1]
	v_pk_fma_f32 v[28:29], v[28:29], v[28:29], v[30:31]
	v_mul_f32_e32 v30, v44, v44
	v_pk_fma_f32 v[30:31], v[44:45], v[44:45], v[30:31] op_sel_hi:[1,1,0]
	v_pk_add_f32 v[46:47], v[18:19], v[24:25] op_sel_hi:[1,0] neg_lo:[0,1] neg_hi:[0,1]
	v_pk_add_f32 v[48:49], v[20:21], v[24:25] op_sel_hi:[1,0] neg_lo:[0,1] neg_hi:[0,1]
	v_mul_f32_e32 v30, v46, v46
	v_pk_add_f32 v[50:51], v[22:23], v[24:25] op_sel_hi:[1,0] neg_lo:[0,1] neg_hi:[0,1]
	v_pk_fma_f32 v[32:33], v[46:47], v[46:47], v[30:31] op_sel_hi:[1,1,0]
	v_pk_mul_f32 v[34:35], v[48:49], v[48:49]
	v_pk_add_f32 v[26:27], v[26:27], v[26:27] op_sel_hi:[0,1]
	v_pk_add_f32 v[28:29], v[28:29], v[28:29] op_sel_hi:[0,1]
	v_pk_mul_f32 v[24:25], v[50:51], v[50:51]
	v_mov_b32_e32 v30, v34
	v_mov_b32_e32 v32, v35
	v_mov_b32_e32 v26, v24
	v_mov_b32_e32 v28, v25
	v_pk_add_f32 v[30:31], v[30:31], v[32:33]
	v_pk_add_f32 v[24:25], v[26:27], v[28:29]
	s_nop 0
	v_pk_add_f32 v[24:25], v[30:31], v[24:25]
	s_nop 0
	v_add_f32_e32 v1, v24, v25
	v_mov_b32_e32 v24, v1
	s_waitcnt lgkmcnt(0)
	s_nop 1
	v_permlane32_swap_b32_e32 v1, v24
	v_add_f32_e32 v1, v1, v24
	v_mov_b32_e32 v24, v1
	s_waitcnt lgkmcnt(0)
	s_nop 1
	v_permlane16_swap_b32_e32 v1, v24
	v_add_f32_e32 v1, v1, v24
	s_waitcnt lgkmcnt(0)
	s_nop 1
	v_add_f32_dpp v1, v1, v1 row_ror:8 row_mask:0xf bank_mask:0xf
	s_waitcnt lgkmcnt(0)
	s_nop 1
	v_add_f32_dpp v1, v1, v1 row_ror:4 row_mask:0xf bank_mask:0xf
	global_load_dwordx4 v[24:27], v0, s[10:11]
	global_load_dwordx4 v[28:31], v0, s[10:11] offset:1024
	s_waitcnt lgkmcnt(0)
	s_nop 1
	v_add_f32_dpp v1, v1, v1 row_ror:2 row_mask:0xf bank_mask:0xf
	global_store_dwordx4 v[6:7], v[8:11], off sc1
	global_store_dwordx4 v[6:7], v[12:15], off offset:1024 sc1
	global_store_dwordx4 v[6:7], v[16:19], off offset:2048 sc1
	global_store_dwordx4 v[6:7], v[20:23], off offset:3072 sc1
	s_waitcnt lgkmcnt(0)
	s_nop 1
	v_add_f32_dpp v1, v1, v1 row_ror:1 row_mask:0xf bank_mask:0xf
	v_mov_b32_e32 v32, 0x3727c5ac
	v_fmac_f32_e32 v32, 0x3a800000, v1
	v_mul_f32_e32 v1, 0x4f800000, v32
	v_cmp_gt_f32_e32 vcc, s0, v32
	global_load_dwordx4 v[12:15], v0, s[4:5]
	global_load_dwordx4 v[16:19], v0, s[4:5] offset:1024
	v_cndmask_b32_e32 v1, v32, v1, vcc
	v_sqrt_f32_e32 v32, v1
	global_load_dwordx4 v[8:11], v0, s[10:11] offset:2048
	v_add_u32_e32 v6, -1, v32
	v_fma_f32 v7, -v6, v32, v1
	v_cmp_ge_f32_e64 s[0:1], 0, v7
	v_add_u32_e32 v7, 1, v32
	v_fma_f32 v20, -v7, v32, v1
	v_cndmask_b32_e64 v6, v32, v6, s[0:1]
	v_cmp_lt_f32_e64 s[0:1], 0, v20
	global_load_dwordx4 v[20:23], v0, s[4:5] offset:2048
	s_nop 0
	v_cndmask_b32_e64 v6, v6, v7, s[0:1]
	v_mul_f32_e32 v7, 0x37800000, v6
	v_cndmask_b32_e32 v6, v6, v7, vcc
	v_mov_b32_e32 v7, 0x260
	v_cmp_class_f32_e32 vcc, v1, v7
	s_nop 1
	v_cndmask_b32_e32 v1, v6, v1, vcc
	v_div_scale_f32 v32, s[0:1], v1, v1, 1.0
	v_rcp_f32_e32 v33, v32
	v_lshl_add_u64 v[6:7], v[2:3], 0, v[4:5]
	v_div_scale_f32 v34, vcc, 1.0, v1, 1.0
	v_fma_f32 v2, -v32, v33, 1.0
	v_fmac_f32_e32 v33, v2, v33
	v_mul_f32_e32 v35, v34, v33
	v_fma_f32 v2, -v32, v35, v34
	v_fmac_f32_e32 v35, v2, v33
	v_fma_f32 v32, -v32, v35, v34
	global_load_dwordx4 v[2:5], v0, s[10:11] offset:3072
	v_div_fmas_f32 v52, v32, v33, v35
	global_load_dwordx4 v[32:35], v0, s[4:5] offset:3072
	v_div_fixup_f32 v0, v52, v1, 1.0
	v_pk_mul_f32 v[36:37], v[36:37], v[0:1] op_sel_hi:[1,0]
	s_waitcnt vmcnt(5)
	v_pk_fma_f32 v[12:13], v[24:25], v[36:37], v[12:13]
	v_pk_mul_f32 v[24:25], v[38:39], v[0:1] op_sel_hi:[1,0]
	v_cvt_pk_f16_f32 v12, v12, v13
	v_pk_fma_f32 v[14:15], v[26:27], v[24:25], v[14:15]
	s_nop 0
	v_cvt_pk_f16_f32 v13, v14, v15
	global_store_dwordx2 v[6:7], v[12:13], off sc1
	v_pk_mul_f32 v[12:13], v[40:41], v[0:1] op_sel_hi:[1,0]
	v_pk_mul_f32 v[14:15], v[42:43], v[0:1] op_sel_hi:[1,0]
	s_waitcnt vmcnt(5)
	v_pk_fma_f32 v[12:13], v[28:29], v[12:13], v[16:17]
	v_pk_fma_f32 v[14:15], v[30:31], v[14:15], v[18:19]
	v_cvt_pk_f16_f32 v12, v12, v13
	v_cvt_pk_f16_f32 v13, v14, v15
	global_store_dwordx2 v[6:7], v[12:13], off offset:512 sc1
	v_pk_mul_f32 v[12:13], v[44:45], v[0:1] op_sel_hi:[1,0]
	s_waitcnt vmcnt(4)
	v_pk_fma_f32 v[8:9], v[12:13], v[8:9], v[20:21]
	v_pk_mul_f32 v[12:13], v[46:47], v[0:1] op_sel_hi:[1,0]
	v_cvt_pk_f16_f32 v8, v8, v9
	v_pk_fma_f32 v[10:11], v[12:13], v[10:11], v[22:23]
	s_nop 0
	v_cvt_pk_f16_f32 v9, v10, v11
	global_store_dwordx2 v[6:7], v[8:9], off offset:1024 sc1
	v_pk_mul_f32 v[8:9], v[48:49], v[0:1] op_sel_hi:[1,0]
	v_pk_mul_f32 v[0:1], v[50:51], v[0:1] op_sel_hi:[1,0]
	s_waitcnt vmcnt(3)
	v_pk_fma_f32 v[2:3], v[8:9], v[2:3], v[32:33]
	v_pk_fma_f32 v[0:1], v[0:1], v[4:5], v[34:35]
	v_cvt_pk_f16_f32 v2, v2, v3
	v_cvt_pk_f16_f32 v3, v0, v1
	global_store_dwordx2 v[6:7], v[2:3], off offset:1536 sc1
	s_endpgm
	s_endpgm
	s_endpgm
	s_endpgm
	s_endpgm
	s_endpgm
	s_endpgm
	s_endpgm
	s_endpgm
	s_endpgm
	s_endpgm
	s_endpgm
	s_endpgm
	s_endpgm
	s_endpgm
	s_endpgm
	s_endpgm
	s_endpgm
	s_endpgm
	s_endpgm
	s_endpgm
	s_endpgm
	s_endpgm
	s_endpgm
	s_endpgm
	s_endpgm
	s_endpgm
	s_endpgm
	s_endpgm
	s_endpgm
	s_endpgm
	s_endpgm
	s_endpgm
	s_endpgm
	s_endpgm
	s_endpgm
	s_endpgm
	s_endpgm
	s_endpgm
	s_endpgm
	s_endpgm
	s_endpgm
	s_endpgm
	s_endpgm
	s_endpgm
	s_endpgm
	s_endpgm
	s_endpgm
	s_endpgm

_Z9ln_kernelILi0EEvPKiPKfS3_PfS3_S3_PDF16_:
	s_load_dwordx8 s[4:11], s[0:1], 0x18
	v_and_b32_e32 v52, 63, v0
	v_lshrrev_b32_e32 v0, 6, v0
	v_lshl_or_b32 v0, s2, 2, v0
	v_ashrrev_i32_e32 v1, 31, v0
	v_lshlrev_b64 v[2:3], 12, v[0:1]
	s_waitcnt lgkmcnt(0)
	v_lshl_add_u64 v[4:5], s[4:5], 0, v[2:3]
	v_lshlrev_b32_e32 v2, 4, v52
	v_mov_b32_e32 v3, 0
	v_lshl_add_u64 v[20:21], v[4:5], 0, v[2:3]
	global_load_dwordx4 v[4:7], v[20:21], off offset:1024
	global_load_dwordx4 v[8:11], v[20:21], off offset:2048
	global_load_dwordx4 v[12:15], v[20:21], off
	global_load_dwordx4 v[16:19], v[20:21], off offset:3072
	v_mbcnt_lo_u32_b32 v20, -1, 0
	v_mbcnt_hi_u32_b32 v32, -1, v20
	v_and_b32_e32 v20, 64, v32
	v_xor_b32_e32 v21, 32, v32
	v_add_u32_e32 v34, 64, v20
	v_cmp_lt_i32_e32 vcc, v21, v34
	v_xor_b32_e32 v33, 16, v32
	s_mov_b32 s0, 0xf800000
	v_cndmask_b32_e32 v20, v32, v21, vcc
	v_lshlrev_b32_e32 v53, 2, v20
	v_cmp_lt_i32_e32 vcc, v33, v34
	v_lshlrev_b64 v[0:1], 11, v[0:1]
	v_lshl_add_u64 v[0:1], s[10:11], 0, v[0:1]
	s_waitcnt vmcnt(3)
	v_mov_b32_e32 v36, v5
	v_mov_b32_e32 v37, v6
	v_mov_b32_e32 v5, v7
	s_waitcnt vmcnt(1)
	v_mov_b32_e32 v22, v12
	v_mov_b32_e32 v23, v14
	v_mov_b32_e32 v24, v13
	v_mov_b32_e32 v25, v15
	v_mov_b32_e32 v6, v9
	v_mov_b32_e32 v20, v11
	s_waitcnt vmcnt(0)
	v_mov_b32_e32 v21, v16
	v_pk_add_f32 v[26:27], v[36:37], v[4:5]
	v_pk_add_f32 v[22:23], v[22:23], v[24:25]
	v_pk_add_f32 v[28:29], v[8:9], v[6:7]
	v_pk_add_f32 v[30:31], v[10:11], v[20:21]
	v_pk_add_f32 v[24:25], v[26:27], v[26:27] op_sel:[0,1] op_sel_hi:[1,0]
	v_add_f32_e32 v5, v22, v23
	v_mov_b32_e32 v29, v18
	v_mov_b32_e32 v31, v19
	v_add_f32_e32 v20, 0, v5
	v_mov_b32_e32 v25, v17
	v_pk_add_f32 v[22:23], v[28:29], v[30:31]
	v_pk_add_f32 v[20:21], v[20:21], v[24:25]
	v_pk_mov_b32 v[36:37], v[36:37], v[36:37] op_sel:[1,0]
	v_pk_add_f32 v[20:21], v[20:21], v[22:23]
	s_nop 0
	v_add_f32_e32 v5, v20, v21
	v_mov_b32_e32 v6, v5
	v_cndmask_b32_e32 v21, v32, v33, vcc
	v_lshlrev_b32_e32 v54, 2, v21
	v_xor_b32_e32 v20, 8, v32
	v_cmp_lt_i32_e32 vcc, v20, v34
	s_waitcnt lgkmcnt(0)
	s_nop 1
	v_permlane32_swap_b32_e32 v5, v6
	v_add_f32_e32 v5, v5, v6
	v_mov_b32_e32 v6, v5
	v_cndmask_b32_e32 v20, v32, v20, vcc
	v_lshlrev_b32_e32 v55, 2, v20
	v_xor_b32_e32 v21, 4, v32
	v_cmp_lt_i32_e32 vcc, v21, v34
	s_waitcnt lgkmcnt(0)
	s_nop 1
	v_permlane16_swap_b32_e32 v5, v6
	v_add_f32_e32 v5, v5, v6
	v_cndmask_b32_e32 v21, v32, v21, vcc
	v_lshlrev_b32_e32 v56, 2, v21
	v_xor_b32_e32 v20, 2, v32
	v_cmp_lt_i32_e32 vcc, v20, v34
	s_waitcnt lgkmcnt(0)
	s_nop 1
	v_add_f32_dpp v5, v5, v5 row_ror:8 row_mask:0xf bank_mask:0xf
	v_cndmask_b32_e32 v20, v32, v20, vcc
	v_lshlrev_b32_e32 v57, 2, v20
	v_xor_b32_e32 v21, 1, v32
	v_cmp_lt_i32_e32 vcc, v21, v34
	s_waitcnt lgkmcnt(0)
	s_nop 1
	v_add_f32_dpp v5, v5, v5 row_ror:4 row_mask:0xf bank_mask:0xf
	v_cndmask_b32_e32 v20, v32, v21, vcc
	v_lshlrev_b32_e32 v58, 2, v20
	global_load_dwordx4 v[20:23], v2, s[6:7]
	global_load_dwordx4 v[24:27], v2, s[8:9]
	global_load_dwordx4 v[28:31], v2, s[6:7] offset:1024
	global_load_dwordx4 v[32:35], v2, s[8:9] offset:1024
	s_waitcnt lgkmcnt(0)
	s_nop 1
	v_add_f32_dpp v6, v5, v5 row_ror:2 row_mask:0xf bank_mask:0xf
	v_mov_b32_e32 v5, v37
	v_mov_b32_e32 v37, v7
	s_waitcnt lgkmcnt(0)
	s_nop 1
	v_add_f32_dpp v6, v6, v6 row_ror:1 row_mask:0xf bank_mask:0xf
	v_mul_f32_e32 v6, 0x3a800000, v6
	v_pk_add_f32 v[38:39], v[12:13], v[6:7] op_sel_hi:[1,0] neg_lo:[0,1] neg_hi:[0,1]
	v_pk_add_f32 v[40:41], v[14:15], v[6:7] op_sel_hi:[1,0] neg_lo:[0,1] neg_hi:[0,1]
	v_pk_add_f32 v[46:47], v[4:5], v[6:7] op_sel_hi:[1,0] neg_lo:[0,1] neg_hi:[0,1]
	v_pk_add_f32 v[36:37], v[36:37], v[6:7] op_sel_hi:[1,0] neg_lo:[0,1] neg_hi:[0,1]
	v_pk_add_f32 v[42:43], v[16:17], v[6:7] op_sel_hi:[1,0] neg_lo:[0,1] neg_hi:[0,1]
	v_pk_add_f32 v[44:45], v[18:19], v[6:7] op_sel_hi:[1,0] neg_lo:[0,1] neg_hi:[0,1]
	v_pk_add_f32 v[48:49], v[8:9], v[6:7] op_sel_hi:[1,0] neg_lo:[0,1] neg_hi:[0,1]
	v_pk_add_f32 v[50:51], v[10:11], v[6:7] op_sel_hi:[1,0] neg_lo:[0,1] neg_hi:[0,1]
	v_mov_b32_e32 v6, v39
	v_mov_b32_e32 v7, v41
	v_mov_b32_e32 v14, v47
	v_mov_b32_e32 v15, v37
	v_mov_b32_e32 v4, v38
	v_mov_b32_e32 v5, v40
	v_mov_b32_e32 v12, v46
	v_mov_b32_e32 v13, v36
	v_pk_mul_f32 v[6:7], v[6:7], v[6:7]
	v_pk_mul_f32 v[14:15], v[14:15], v[14:15]
	v_mul_f32_e32 v16, v48, v48
	v_mul_f32_e32 v18, v50, v50
	v_pk_fma_f32 v[4:5], v[4:5], v[4:5], v[6:7]
	v_pk_fma_f32 v[6:7], v[12:13], v[12:13], v[14:15]
	v_pk_mul_f32 v[8:9], v[42:43], v[42:43]
	v_pk_mul_f32 v[10:11], v[44:45], v[44:45]
	v_pk_fma_f32 v[16:17], v[48:49], v[48:49], v[16:17] op_sel_hi:[1,1,0]
	v_pk_fma_f32 v[18:19], v[50:51], v[50:51], v[18:19] op_sel_hi:[1,1,0]
	v_pk_add_f32 v[4:5], v[4:5], v[4:5] op_sel_hi:[0,1]
	v_pk_add_f32 v[6:7], v[6:7], v[6:7] op_sel_hi:[0,1]
	v_mov_b32_e32 v16, v8
	v_mov_b32_e32 v18, v9
	v_mov_b32_e32 v4, v10
	v_mov_b32_e32 v6, v11
	v_pk_add_f32 v[8:9], v[16:17], v[18:19]
	v_pk_add_f32 v[4:5], v[4:5], v[6:7]
	s_nop 0
	v_pk_add_f32 v[4:5], v[8:9], v[4:5]
	s_nop 0
	v_add_f32_e32 v59, v4, v5
	global_load_dwordx4 v[4:7], v2, s[6:7] offset:2048
	global_load_dwordx4 v[8:11], v2, s[8:9] offset:2048
	global_load_dwordx4 v[12:15], v2, s[6:7] offset:3072
	global_load_dwordx4 v[16:19], v2, s[8:9] offset:3072
	v_mov_b32_e32 v53, v59
	s_waitcnt lgkmcnt(0)
	s_nop 1
	v_permlane32_swap_b32_e32 v59, v53
	v_add_f32_e32 v2, v59, v53
	v_mov_b32_e32 v53, v2
	v_mov_b32_e32 v54, 0x3727c5ac
	s_waitcnt lgkmcnt(0)
	s_nop 1
	v_permlane16_swap_b32_e32 v2, v53
	v_add_f32_e32 v2, v2, v53
	v_mov_b32_e32 v55, 0x260
	s_waitcnt lgkmcnt(0)
	s_nop 1
	v_add_f32_dpp v2, v2, v2 row_ror:8 row_mask:0xf bank_mask:0xf
	s_waitcnt lgkmcnt(0)
	s_nop 1
	v_add_f32_dpp v2, v2, v2 row_ror:4 row_mask:0xf bank_mask:0xf
	s_waitcnt lgkmcnt(0)
	s_nop 1
	v_add_f32_dpp v2, v2, v2 row_ror:2 row_mask:0xf bank_mask:0xf
	s_waitcnt lgkmcnt(0)
	s_nop 1
	v_add_f32_dpp v2, v2, v2 row_ror:1 row_mask:0xf bank_mask:0xf
	v_fmac_f32_e32 v54, 0x3a800000, v2
	v_mul_f32_e32 v2, 0x4f800000, v54
	v_cmp_gt_f32_e32 vcc, s0, v54
	s_nop 1
	v_cndmask_b32_e32 v53, v54, v2, vcc
	v_sqrt_f32_e32 v54, v53
	v_lshlrev_b32_e32 v2, 3, v52
	v_lshl_add_u64 v[0:1], v[0:1], 0, v[2:3]
	v_add_u32_e32 v52, -1, v54
	v_add_u32_e32 v56, 1, v54
	v_fma_f32 v57, -v52, v54, v53
	v_fma_f32 v58, -v56, v54, v53
	v_cmp_ge_f32_e64 s[0:1], 0, v57
	s_nop 1
	v_cndmask_b32_e64 v52, v54, v52, s[0:1]
	v_cmp_lt_f32_e64 s[0:1], 0, v58
	s_nop 1
	v_cndmask_b32_e64 v52, v52, v56, s[0:1]
	v_mul_f32_e32 v54, 0x37800000, v52
	v_cndmask_b32_e32 v52, v52, v54, vcc
	v_cmp_class_f32_e32 vcc, v53, v55
	s_nop 1
	v_cndmask_b32_e32 v52, v52, v53, vcc
	v_div_scale_f32 v53, s[0:1], v52, v52, 1.0
	v_rcp_f32_e32 v54, v53
	v_div_scale_f32 v2, vcc, 1.0, v52, 1.0
	v_fma_f32 v3, -v53, v54, 1.0
	v_fmac_f32_e32 v54, v3, v54
	v_mul_f32_e32 v3, v2, v54
	v_fma_f32 v55, -v53, v3, v2
	v_fmac_f32_e32 v3, v55, v54
	v_fma_f32 v2, -v53, v3, v2
	v_div_fmas_f32 v2, v2, v54, v3
	v_div_fixup_f32 v2, v2, v52, 1.0
	v_pk_mul_f32 v[38:39], v[38:39], v[2:3] op_sel_hi:[1,0]
	v_pk_mul_f32 v[40:41], v[40:41], v[2:3] op_sel_hi:[1,0]
	v_pk_mul_f32 v[46:47], v[46:47], v[2:3] op_sel_hi:[1,0]
	v_pk_mul_f32 v[36:37], v[36:37], v[2:3] op_sel_hi:[1,0]
	v_pk_mul_f32 v[48:49], v[48:49], v[2:3] op_sel_hi:[1,0]
	v_pk_mul_f32 v[50:51], v[50:51], v[2:3] op_sel_hi:[1,0]
	v_pk_mul_f32 v[42:43], v[42:43], v[2:3] op_sel_hi:[1,0]
	v_pk_mul_f32 v[2:3], v[44:45], v[2:3] op_sel_hi:[1,0]
	s_waitcnt vmcnt(6)
	v_pk_fma_f32 v[20:21], v[20:21], v[38:39], v[24:25]
	v_pk_fma_f32 v[22:23], v[22:23], v[40:41], v[26:27]
	s_waitcnt vmcnt(4)
	v_pk_fma_f32 v[24:25], v[28:29], v[46:47], v[32:33]
	v_pk_fma_f32 v[26:27], v[30:31], v[36:37], v[34:35]
	s_waitcnt vmcnt(2)
	v_pk_fma_f32 v[4:5], v[48:49], v[4:5], v[8:9]
	v_pk_fma_f32 v[6:7], v[50:51], v[6:7], v[10:11]
	s_waitcnt vmcnt(0)
	v_pk_fma_f32 v[8:9], v[42:43], v[12:13], v[16:17]
	v_pk_fma_f32 v[2:3], v[2:3], v[14:15], v[18:19]
	v_cvt_pk_f16_f32 v10, v20, v21
	v_cvt_pk_f16_f32 v11, v22, v23
	v_cvt_pk_f16_f32 v12, v24, v25
	v_cvt_pk_f16_f32 v13, v26, v27
	v_cvt_pk_f16_f32 v4, v4, v5
	v_cvt_pk_f16_f32 v5, v6, v7
	v_cvt_pk_f16_f32 v6, v8, v9
	v_cvt_pk_f16_f32 v7, v2, v3
	global_store_dwordx2 v[0:1], v[10:11], off sc1
	global_store_dwordx2 v[0:1], v[12:13], off offset:512 sc1
	global_store_dwordx2 v[0:1], v[4:5], off offset:1024 sc1
	global_store_dwordx2 v[0:1], v[6:7], off offset:1536 sc1
	s_endpgm
	s_endpgm
	s_endpgm
	s_endpgm
	s_endpgm
	s_endpgm
	s_endpgm
	s_endpgm
	s_endpgm
	s_endpgm
	s_endpgm
	s_endpgm
	s_endpgm
	s_endpgm
	s_endpgm
	s_endpgm
	s_endpgm
	s_endpgm
	s_endpgm
	s_endpgm
	s_endpgm
	s_endpgm
	s_endpgm
	s_endpgm
	s_endpgm
	s_endpgm
	s_endpgm
	s_endpgm
	s_endpgm
	s_endpgm
	s_endpgm
	s_endpgm
	s_endpgm
	s_endpgm
	s_endpgm
	s_endpgm
	s_endpgm
	s_endpgm
	s_endpgm
	s_endpgm

_Z9ln_kernelILi4EEvPKiPKfS3_PfS3_S3_PDF16_:
	s_load_dwordx8 s[4:11], s[0:1], 0x8
	v_and_b32_e32 v12, 63, v0
	v_lshrrev_b32_e32 v0, 6, v0
	v_lshl_or_b32 v0, s2, 2, v0
	v_ashrrev_i32_e32 v1, 31, v0
	v_lshlrev_b64 v[24:25], 11, v[0:1]
	v_mov_b32_e32 v29, 0
	s_waitcnt lgkmcnt(0)
	v_lshl_add_u64 v[2:3], s[4:5], 0, v[24:25]
	v_lshlrev_b32_e32 v26, 3, v12
	v_mov_b32_e32 v27, v29
	v_lshl_add_u64 v[4:5], v[2:3], 0, v[26:27]
	s_mov_b64 s[2:3], 0x400000
	v_lshl_add_u64 v[10:11], v[4:5], 0, s[2:3]
	global_load_dwordx2 v[6:7], v[4:5], off offset:512
	global_load_dwordx2 v[8:9], v[4:5], off
	global_load_dwordx2 v[46:47], v[10:11], off offset:512
	s_mov_b32 s2, 0x400000
	v_add_co_u32_e32 v2, vcc, s2, v4
	v_lshlrev_b64 v[0:1], 12, v[0:1]
	s_nop 0
	v_addc_co_u32_e32 v3, vcc, 0, v5, vcc
	global_load_dwordx2 v[48:49], v[2:3], off
	v_lshl_add_u64 v[0:1], s[8:9], 0, v[0:1]
	v_lshlrev_b32_e32 v28, 4, v12
	v_lshl_add_u64 v[50:51], v[0:1], 0, v[28:29]
	global_load_dwordx4 v[0:3], v[50:51], off
	global_load_dwordx4 v[34:37], v28, s[6:7] offset:1024
	global_load_dwordx4 v[38:41], v[50:51], off offset:1024
	global_load_dwordx2 v[52:53], v[4:5], off offset:1024
	global_load_dwordx2 v[54:55], v[10:11], off offset:1024
	global_load_dwordx2 v[32:33], v[4:5], off offset:1536
	global_load_dwordx2 v[30:31], v[10:11], off offset:1536
	global_load_dwordx4 v[16:19], v[50:51], off offset:2048
	global_load_dwordx4 v[42:45], v28, s[6:7]
	global_load_dwordx4 v[20:23], v28, s[6:7] offset:2048
	global_load_dwordx4 v[12:15], v[50:51], off offset:3072
	global_load_dwordx4 v[60:63], v28, s[6:7] offset:3072
	s_load_dwordx4 s[4:7], s[0:1], 0x28
	s_mov_b32 s0, 0xf800000
	s_waitcnt lgkmcnt(0)
	v_lshl_add_u64 v[24:25], s[6:7], 0, v[24:25]
	v_lshl_add_u64 v[24:25], v[24:25], 0, v[26:27]
	s_waitcnt vmcnt(15)
	v_cvt_f32_f16_e32 v4, v6
	v_cvt_f32_f16_sdwa v5, v6 dst_sel:DWORD dst_unused:UNUSED_PAD src0_sel:WORD_1
	v_cvt_f32_f16_e32 v56, v7
	v_cvt_f32_f16_sdwa v57, v7 dst_sel:DWORD dst_unused:UNUSED_PAD src0_sel:WORD_1
	s_waitcnt vmcnt(13)
	v_cvt_f32_f16_e32 v6, v46
	v_cvt_f32_f16_sdwa v7, v46 dst_sel:DWORD dst_unused:UNUSED_PAD src0_sel:WORD_1
	v_cvt_f32_f16_e32 v58, v47
	v_cvt_f32_f16_sdwa v59, v47 dst_sel:DWORD dst_unused:UNUSED_PAD src0_sel:WORD_1
	v_cvt_f32_f16_e32 v10, v8
	v_pk_add_f32 v[50:51], v[4:5], v[6:7]
	v_add_f32_e32 v58, v56, v58
	v_add_f32_e32 v57, v57, v59
	s_waitcnt vmcnt(10)
	v_mov_b32_e32 v56, v37
	s_waitcnt vmcnt(9)
	v_pk_add_f32 v[38:39], v[38:39], v[50:51]
	v_add_f32_e32 v37, v40, v58
	v_add_f32_e32 v40, v41, v57
	s_waitcnt vmcnt(8)
	v_cvt_f32_f16_e32 v41, v52
	v_cvt_f32_f16_sdwa v50, v52 dst_sel:DWORD dst_unused:UNUSED_PAD src0_sel:WORD_1
	s_waitcnt vmcnt(7)
	v_cvt_f32_f16_e32 v52, v54
	v_cvt_f32_f16_sdwa v11, v8 dst_sel:DWORD dst_unused:UNUSED_PAD src0_sel:WORD_1
	v_cvt_f32_f16_e32 v46, v48
	v_cvt_f32_f16_sdwa v47, v48 dst_sel:DWORD dst_unused:UNUSED_PAD src0_sel:WORD_1
	v_cvt_f32_f16_e32 v8, v9
	v_cvt_f32_f16_sdwa v9, v9 dst_sel:DWORD dst_unused:UNUSED_PAD src0_sel:WORD_1
	v_cvt_f32_f16_e32 v48, v49
	v_cvt_f32_f16_sdwa v49, v49 dst_sel:DWORD dst_unused:UNUSED_PAD src0_sel:WORD_1
	v_cvt_f32_f16_e32 v51, v53
	v_cvt_f32_f16_sdwa v53, v53 dst_sel:DWORD dst_unused:UNUSED_PAD src0_sel:WORD_1
	v_pk_add_f32 v[34:35], v[34:35], v[38:39]
	v_add_f32_e32 v36, v36, v37
	v_cvt_f32_f16_sdwa v37, v54 dst_sel:DWORD dst_unused:UNUSED_PAD src0_sel:WORD_1
	v_cvt_f32_f16_e32 v38, v55
	v_cvt_f32_f16_sdwa v54, v55 dst_sel:DWORD dst_unused:UNUSED_PAD src0_sel:WORD_1
	s_waitcnt vmcnt(6)
	v_cvt_f32_f16_e32 v39, v32
	v_cvt_f32_f16_sdwa v57, v32 dst_sel:DWORD dst_unused:UNUSED_PAD src0_sel:WORD_1
	v_add_f32_e32 v32, v41, v52
	s_waitcnt vmcnt(4)
	v_add_f32_e32 v16, v16, v32
	v_pk_add_f32 v[46:47], v[10:11], v[46:47]
	s_waitcnt vmcnt(2)
	v_add_f32_e32 v32, v20, v16
	v_mbcnt_lo_u32_b32 v16, -1, 0
	v_pk_add_f32 v[48:49], v[8:9], v[48:49]
	v_pk_add_f32 v[46:47], v[0:1], v[46:47]
	v_add_f32_e32 v38, v51, v38
	v_cvt_f32_f16_e32 v51, v30
	v_cvt_f32_f16_sdwa v41, v30 dst_sel:DWORD dst_unused:UNUSED_PAD src0_sel:WORD_1
	v_add_f32_e32 v30, v53, v54
	v_mbcnt_hi_u32_b32 v54, -1, v16
	v_pk_add_f32 v[48:49], v[2:3], v[48:49]
	v_pk_add_f32 v[42:43], v[42:43], v[46:47]
	v_cvt_f32_f16_e32 v47, v33
	v_cvt_f32_f16_e32 v53, v31
	v_and_b32_e32 v16, 64, v54
	v_pk_add_f32 v[44:45], v[44:45], v[48:49]
	v_cvt_f32_f16_sdwa v49, v33 dst_sel:DWORD dst_unused:UNUSED_PAD src0_sel:WORD_1
	v_cvt_f32_f16_sdwa v31, v31 dst_sel:DWORD dst_unused:UNUSED_PAD src0_sel:WORD_1
	v_add_u32_e32 v55, 64, v16
	v_xor_b32_e32 v16, 32, v54
	v_cmp_lt_i32_e32 vcc, v16, v55
	v_add_f32_e32 v52, v50, v37
	v_add_f32_e32 v18, v18, v38
	v_cndmask_b32_e32 v16, v54, v16, vcc
	v_mov_b32_e32 v46, v17
	v_mov_b32_e32 v38, v44
	v_mov_b32_e32 v50, v45
	v_lshlrev_b32_e32 v58, 2, v16
	v_pk_add_f32 v[16:17], v[46:47], v[52:53]
	v_mov_b32_e32 v20, v21
	s_waitcnt vmcnt(1)
	v_mov_b32_e32 v21, v14
	v_mov_b32_e32 v48, v19
	v_pk_add_f32 v[38:39], v[38:39], v[50:51]
	v_pk_add_f32 v[50:51], v[42:43], v[42:43] op_sel:[0,1] op_sel_hi:[1,0]
	v_pk_add_f32 v[40:41], v[56:57], v[40:41]
	v_pk_add_f32 v[20:21], v[20:21], v[16:17]
	v_pk_add_f32 v[16:17], v[48:49], v[30:31]
	v_mov_b32_e32 v14, v23
	v_mov_b32_e32 v37, v13
	v_pk_add_f32 v[46:47], v[34:35], v[34:35] op_sel:[0,1] op_sel_hi:[1,0]
	v_mov_b32_e32 v51, v12
	v_add_f32_e32 v22, v22, v18
	v_pk_add_f32 v[30:31], v[14:15], v[16:17]
	v_pk_add_f32 v[18:19], v[36:37], v[40:41]
	s_waitcnt vmcnt(0)
	v_mov_b32_e32 v47, v61
	v_mov_b32_e32 v33, v62
	v_mov_b32_e32 v23, v63
	v_pk_add_f32 v[12:13], v[50:51], v[38:39]
	v_mov_b32_e32 v38, v29
	v_mov_b32_e32 v39, v60
	v_pk_add_f32 v[46:47], v[46:47], v[18:19]
	v_pk_add_f32 v[48:49], v[32:33], v[20:21]
	v_pk_add_f32 v[52:53], v[22:23], v[30:31]
	v_pk_add_f32 v[12:13], v[38:39], v[12:13]
	v_pk_add_f32 v[18:19], v[48:49], v[52:53]
	v_pk_add_f32 v[38:39], v[12:13], v[46:47]
	v_mov_b32_e32 v37, v40
	v_pk_add_f32 v[18:19], v[38:39], v[18:19]
	v_mov_b32_e32 v33, v20
	v_add_f32_e32 v12, v18, v19
	v_mov_b32_e32 v18, v12
	v_xor_b32_e32 v19, 16, v54
	v_cmp_lt_i32_e32 vcc, v19, v55
	v_mov_b32_e32 v23, v30
	v_mov_b32_e32 v46, v13
	v_cndmask_b32_e32 v19, v54, v19, vcc
	v_lshlrev_b32_e32 v29, 2, v19
	s_waitcnt lgkmcnt(0)
	s_nop 1
	v_permlane32_swap_b32_e32 v12, v18
	v_add_f32_e32 v12, v12, v18
	v_mov_b32_e32 v18, v12
	v_xor_b32_e32 v19, 8, v54
	v_cmp_lt_i32_e32 vcc, v19, v55
	v_mov_b32_e32 v52, v49
	global_load_dwordx4 v[4:7], v28, s[10:11]
	global_load_dwordx4 v[8:11], v28, s[10:11] offset:1024
	v_cndmask_b32_e32 v19, v54, v19, vcc
	v_lshlrev_b32_e32 v48, 2, v19
	s_waitcnt lgkmcnt(0)
	s_nop 1
	v_permlane16_swap_b32_e32 v12, v18
	v_add_f32_e32 v12, v12, v18
	v_xor_b32_e32 v19, 4, v54
	v_cmp_lt_i32_e32 vcc, v19, v55
	global_load_dwordx4 v[0:3], v28, s[10:11] offset:2048
	global_load_dwordx4 v[14:17], v28, s[10:11] offset:3072
	v_cndmask_b32_e32 v19, v54, v19, vcc
	v_lshlrev_b32_e32 v59, 2, v19
	s_waitcnt lgkmcnt(0)
	s_nop 1
	v_add_f32_dpp v12, v12, v12 row_ror:8 row_mask:0xf bank_mask:0xf
	v_xor_b32_e32 v19, 2, v54
	v_cmp_lt_i32_e32 vcc, v19, v55
	s_waitcnt lgkmcnt(0)
	s_nop 1
	v_add_f32_dpp v12, v12, v12 row_ror:4 row_mask:0xf bank_mask:0xf
	v_cndmask_b32_e32 v19, v54, v19, vcc
	v_lshlrev_b32_e32 v60, 2, v19
	v_xor_b32_e32 v19, 1, v54
	v_cmp_lt_i32_e32 vcc, v19, v55
	s_waitcnt lgkmcnt(0)
	s_nop 1
	v_add_f32_dpp v12, v12, v12 row_ror:2 row_mask:0xf bank_mask:0xf
	v_cndmask_b32_e32 v19, v54, v19, vcc
	v_lshlrev_b32_e32 v61, 2, v19
	s_waitcnt lgkmcnt(0)
	s_nop 1
	v_add_f32_dpp v12, v12, v12 row_ror:1 row_mask:0xf bank_mask:0xf
	v_mul_f32_e32 v12, 0x3a800000, v12
	v_pk_add_f32 v[42:43], v[42:43], v[12:13] op_sel_hi:[1,0] neg_lo:[0,1] neg_hi:[0,1]
	v_pk_add_f32 v[44:45], v[44:45], v[12:13] op_sel_hi:[1,0] neg_lo:[0,1] neg_hi:[0,1]
	v_mov_b32_e32 v38, v43
	v_mov_b32_e32 v39, v45
	v_pk_add_f32 v[50:51], v[34:35], v[12:13] op_sel_hi:[1,0] neg_lo:[0,1] neg_hi:[0,1]
	v_pk_add_f32 v[54:55], v[36:37], v[12:13] op_sel_hi:[1,0] neg_lo:[0,1] neg_hi:[0,1]
	v_pk_add_f32 v[56:57], v[32:33], v[12:13] op_sel_hi:[1,0] neg_lo:[0,1] neg_hi:[0,1]
	v_mov_b32_e32 v18, v42
	v_mov_b32_e32 v19, v44
	v_pk_mul_f32 v[38:39], v[38:39], v[38:39]
	v_mov_b32_e32 v34, v51
	v_mov_b32_e32 v35, v55
	v_mul_f32_e32 v30, v56, v56
	v_pk_fma_f32 v[38:39], v[18:19], v[18:19], v[38:39]
	v_mov_b32_e32 v18, v50
	v_mov_b32_e32 v19, v54
	v_pk_mul_f32 v[34:35], v[34:35], v[34:35]
	v_pk_fma_f32 v[30:31], v[56:57], v[56:57], v[30:31] op_sel_hi:[1,1,0]
	v_pk_add_f32 v[22:23], v[22:23], v[12:13] op_sel_hi:[1,0] neg_lo:[0,1] neg_hi:[0,1]
	v_pk_fma_f32 v[34:35], v[18:19], v[18:19], v[34:35]
	v_mul_f32_e32 v30, v22, v22
	v_pk_add_f32 v[46:47], v[46:47], v[12:13] op_sel_hi:[1,0] neg_lo:[0,1] neg_hi:[0,1]
	v_pk_add_f32 v[12:13], v[52:53], v[12:13] op_sel_hi:[1,0] neg_lo:[0,1] neg_hi:[0,1]
	v_pk_add_f32 v[36:37], v[38:39], v[38:39] op_sel_hi:[0,1]
	v_pk_add_f32 v[34:35], v[34:35], v[34:35] op_sel_hi:[0,1]
	v_pk_fma_f32 v[32:33], v[22:23], v[22:23], v[30:31] op_sel_hi:[1,1,0]
	v_pk_mul_f32 v[38:39], v[46:47], v[46:47]
	v_pk_mul_f32 v[40:41], v[12:13], v[12:13]
	v_mov_b32_e32 v30, v38
	v_mov_b32_e32 v32, v39
	v_mov_b32_e32 v36, v40
	v_mov_b32_e32 v34, v41
	v_pk_add_f32 v[30:31], v[30:31], v[32:33]
	v_pk_add_f32 v[32:33], v[36:37], v[34:35]
	global_load_dwordx4 v[18:21], v28, s[4:5]
	v_pk_add_f32 v[30:31], v[30:31], v[32:33]
	s_nop 0
	v_add_f32_e32 v34, v30, v31
	v_mov_b32_e32 v35, v34
	global_load_dwordx4 v[30:33], v28, s[4:5] offset:1024
	s_waitcnt lgkmcnt(0)
	s_nop 1
	v_permlane32_swap_b32_e32 v34, v35
	v_add_f32_e32 v38, v34, v35
	v_mov_b32_e32 v29, v38
	global_load_dwordx4 v[34:37], v28, s[4:5] offset:2048
	s_waitcnt lgkmcnt(0)
	s_nop 1
	v_permlane16_swap_b32_e32 v38, v29
	v_add_f32_e32 v29, v38, v29
	global_load_dwordx4 v[38:41], v28, s[4:5] offset:3072
	s_waitcnt lgkmcnt(0)
	s_nop 1
	v_add_f32_dpp v28, v29, v29 row_ror:8 row_mask:0xf bank_mask:0xf
	s_waitcnt lgkmcnt(0)
	s_nop 1
	v_add_f32_dpp v28, v28, v28 row_ror:4 row_mask:0xf bank_mask:0xf
	s_waitcnt lgkmcnt(0)
	s_nop 1
	v_add_f32_dpp v28, v28, v28 row_ror:2 row_mask:0xf bank_mask:0xf
	s_waitcnt lgkmcnt(0)
	s_nop 1
	v_add_f32_dpp v28, v28, v28 row_ror:1 row_mask:0xf bank_mask:0xf
	v_mov_b32_e32 v29, 0x3727c5ac
	v_fmac_f32_e32 v29, 0x3a800000, v28
	v_mul_f32_e32 v28, 0x4f800000, v29
	v_cmp_gt_f32_e32 vcc, s0, v29
	s_nop 1
	v_cndmask_b32_e32 v28, v29, v28, vcc
	v_sqrt_f32_e32 v29, v28
	s_nop 0
	v_add_u32_e32 v48, -1, v29
	v_fma_f32 v49, -v48, v29, v28
	v_cmp_ge_f32_e64 s[0:1], 0, v49
	v_add_u32_e32 v49, 1, v29
	s_nop 0
	v_cndmask_b32_e64 v48, v29, v48, s[0:1]
	v_fma_f32 v29, -v49, v29, v28
	v_cmp_lt_f32_e64 s[0:1], 0, v29
	s_nop 1
	v_cndmask_b32_e64 v29, v48, v49, s[0:1]
	v_mul_f32_e32 v48, 0x37800000, v29
	v_cndmask_b32_e32 v29, v29, v48, vcc
	v_mov_b32_e32 v48, 0x260
	v_cmp_class_f32_e32 vcc, v28, v48
	s_nop 1
	v_cndmask_b32_e32 v28, v29, v28, vcc
	v_div_scale_f32 v29, s[0:1], v28, v28, 1.0
	v_rcp_f32_e32 v48, v29
	s_nop 0
	v_fma_f32 v26, -v29, v48, 1.0
	v_fmac_f32_e32 v48, v26, v48
	v_div_scale_f32 v26, vcc, 1.0, v28, 1.0
	v_mul_f32_e32 v27, v26, v48
	v_fma_f32 v49, -v29, v27, v26
	v_fmac_f32_e32 v27, v49, v48
	v_fma_f32 v26, -v29, v27, v26
	v_div_fmas_f32 v26, v26, v48, v27
	v_div_fixup_f32 v26, v26, v28, 1.0
	v_pk_mul_f32 v[28:29], v[42:43], v[26:27] op_sel_hi:[1,0]
	s_waitcnt vmcnt(3)
	v_pk_fma_f32 v[4:5], v[4:5], v[28:29], v[18:19]
	v_pk_mul_f32 v[18:19], v[44:45], v[26:27] op_sel_hi:[1,0]
	v_cvt_pk_f16_f32 v4, v4, v5
	v_pk_fma_f32 v[6:7], v[6:7], v[18:19], v[20:21]
	s_nop 0
	v_cvt_pk_f16_f32 v5, v6, v7
	global_store_dwordx2 v[24:25], v[4:5], off sc1
	v_pk_mul_f32 v[4:5], v[50:51], v[26:27] op_sel_hi:[1,0]
	v_pk_mul_f32 v[6:7], v[54:55], v[26:27] op_sel_hi:[1,0]
	s_waitcnt vmcnt(3)
	v_pk_fma_f32 v[4:5], v[8:9], v[4:5], v[30:31]
	v_pk_fma_f32 v[6:7], v[10:11], v[6:7], v[32:33]
	v_cvt_pk_f16_f32 v4, v4, v5
	v_cvt_pk_f16_f32 v5, v6, v7
	global_store_dwordx2 v[24:25], v[4:5], off offset:512 sc1
	v_pk_mul_f32 v[4:5], v[56:57], v[26:27] op_sel_hi:[1,0]
	s_waitcnt vmcnt(3)
	v_pk_fma_f32 v[0:1], v[0:1], v[4:5], v[34:35]
	v_pk_mul_f32 v[4:5], v[22:23], v[26:27] op_sel_hi:[1,0]
	v_cvt_pk_f16_f32 v0, v0, v1
	v_pk_fma_f32 v[2:3], v[4:5], v[2:3], v[36:37]
	s_nop 0
	v_cvt_pk_f16_f32 v1, v2, v3
	global_store_dwordx2 v[24:25], v[0:1], off offset:1024 sc1
	v_pk_mul_f32 v[0:1], v[46:47], v[26:27] op_sel_hi:[1,0]
	v_pk_mul_f32 v[2:3], v[12:13], v[26:27] op_sel_hi:[1,0]
	s_waitcnt vmcnt(3)
	v_pk_fma_f32 v[0:1], v[0:1], v[14:15], v[38:39]
	v_pk_fma_f32 v[2:3], v[2:3], v[16:17], v[40:41]
	v_cvt_pk_f16_f32 v0, v0, v1
	v_cvt_pk_f16_f32 v1, v2, v3
	global_store_dwordx2 v[24:25], v[0:1], off offset:1536 sc1
	s_endpgm
	s_endpgm
	s_endpgm
	s_endpgm
	s_endpgm
	s_endpgm
	s_endpgm
	s_endpgm
	s_endpgm
	s_endpgm
	s_endpgm
	s_endpgm
	s_endpgm
	s_endpgm
	s_endpgm
	s_endpgm
	s_endpgm
	s_endpgm
	s_endpgm
